# stack: diff epilogue DPP butterflies, SWA sink-logit load hoisted above the last PV MFMAs, SWA 1/sum row broadcasts batched behind one wait, GLA direction-head extra load merged with the gate loads
# baseline (speedup 1.0000x reference)
; #define LAS __attribute__((address_space(3)))
; __device__ __forceinline__ void gla_load_gates(KP Pk, Frame& F, int l, int h, int dir, LAS unsigned char* wl) {
;     LAS float* gw = (LAS float*)(wl + GL_GW); LAS float* gb = (LAS float*)(wl + GL_GB);
;     const float* src = Pk->in[I_GGW] + ((size_t)(l * 2 + dir) * 16) * 256 + h * 32;
; #pragma unroll
;     for (int i = 0; i < 8; ++i) { const int e = F.lane + 64 * i; gw[e] = src[(e >> 5) * 256 + (e & 31)]; }
;     if (F.lane < 32) gb[F.lane] = Pk->in[I_GGB][(l * 2 + dir) * 256 + h * 32 + F.lane];
; }
.LBB0_644:
	s_load_dwordx2 s[26:27], s[48:49], 0x58
	v_readlane_b32 s5, v254, 42
	s_or_b32 s5, s4, s5
	s_lshl_b32 s60, s5, 12
	s_lshl_b64 s[8:9], s[60:61], 2
	s_add_u32 s8, s96, s8
	s_addc_u32 s9, s97, s9
	v_lshl_add_u64 v[2:3], v[78:79], 2, s[8:9]
	global_load_dword v212, v[2:3], off
	v_lshl_add_u64 v[2:3], v[80:81], 2, s[8:9]
	global_load_dword v213, v[2:3], off
	v_lshl_add_u64 v[2:3], v[82:83], 2, s[8:9]
	global_load_dword v214, v[2:3], off
	v_lshl_add_u64 v[2:3], v[84:85], 2, s[8:9]
	global_load_dword v215, v[2:3], off
	v_lshl_add_u64 v[2:3], v[86:87], 2, s[8:9]
	global_load_dword v216, v[2:3], off
	v_lshl_add_u64 v[2:3], v[88:89], 2, s[8:9]
	global_load_dword v217, v[2:3], off
	v_lshl_add_u64 v[2:3], v[90:91], 2, s[8:9]
	global_load_dword v218, v[2:3], off
	v_lshl_add_u64 v[2:3], v[92:93], 2, s[8:9]
	global_load_dword v219, v[2:3], off
	s_and_saveexec_b64 s[8:9], s[38:39]
	v_lshl_add_u32 v2, s5, 8, v159
	v_ashrrev_i32_e32 v3, 31, v2
	s_waitcnt lgkmcnt(0)
	v_lshl_add_u64 v[2:3], v[2:3], 2, s[26:27]
	global_load_dword v1, v[2:3], off
	s_or_b64 exec, exec, s[8:9]
	s_waitcnt vmcnt(0)
	ds_write2st64_b32 v158, v212, v213 offset0:52 offset1:53
	ds_write2st64_b32 v158, v214, v215 offset0:54 offset1:55
	ds_write2st64_b32 v158, v216, v217 offset0:56 offset1:57
	ds_write2st64_b32 v158, v218, v219 offset0:58 offset1:59
	s_and_saveexec_b64 s[8:9], s[38:39]
	s_cbranch_execz .LBB0_646
	ds_write_b32 v158, v1 offset:15360
